# speedup vs baseline: 1.0071x; 1.0071x over previous
.Lprio_done:
	s_cmp_eq_u32 s3, 3
	v_lshl_add_u32 v0, s3, 17, v217
	v_add_u32_e32 v1, 0x20000, v0
	s_cselect_b64 vcc, -1, 0
	v_cndmask_b32_e32 v0, v1, v0, vcc
	v_or_b32_e32 v0, v0, v215
	v_ashrrev_i32_e32 v1, 31, v0
	v_lshl_add_u64 v[0:1], v[0:1], 2, s[40:41]
	v_mov_b32_e32 v2, v219
	v_mov_b32_e32 v3, v218
	global_load_dword v218, v[0:1], off
	global_load_dword v219, v[0:1], off offset:256
	v_add_f32_e32 v0, v2, v3
	s_nop 1
	v_add_f32_dpp v0, v0, v0 quad_perm:[1,0,3,2] row_mask:0xf bank_mask:0xf bound_ctrl:1
	s_nop 1
	v_add_f32_dpp v0, v0, v0 quad_perm:[2,3,0,1] row_mask:0xf bank_mask:0xf bound_ctrl:1
	s_nop 1
	v_add_f32_dpp v0, v0, v0 row_half_mirror row_mask:0xf bank_mask:0xf bound_ctrl:1
	s_nop 1
	v_add_f32_dpp v0, v0, v0 row_mirror row_mask:0xf bank_mask:0xf bound_ctrl:1
	s_nop 0
	v_readlane_b32 s1, v0, 16
	v_readlane_b32 s9, v0, 48
	v_readlane_b32 s0, v0, 0
	v_readlane_b32 s8, v0, 32
	v_mov_b32_e32 v0, s1
	v_mov_b32_e32 v1, s9
	v_add_f32_e32 v0, s0, v0
	v_add_f32_e32 v1, s8, v1
	v_add_f32_e32 v0, v0, v1
	v_fma_mixlo_f16 v1, v0, s33, v3
	v_fma_mixlo_f16 v0, v0, s33, v2
	ds_write_b16 v220, v1 offset:14
	ds_write_b16 v220, v0 offset:142
	ds_write_b16 v220, v1 offset:300
	ds_write_b16 v220, v0 offset:428
	ds_read2_b32 v[2:3], v223 offset0:2 offset1:3
	ds_read2_b32 v[0:1], v223 offset1:1
	ds_read2_b32 v[4:5], v223 offset0:32 offset1:33
	ds_read2_b32 v[6:7], v223 offset0:34 offset1:35
	s_mov_b32 s8, 0
	s_mov_b32 s9, s8
	s_mov_b32 s10, s8
	s_waitcnt lgkmcnt(3)
	v_or_b32_sdwa v8, v3, s34 dst_sel:DWORD dst_unused:UNUSED_PAD src0_sel:WORD_0 src1_sel:DWORD
	v_cndmask_b32_e64 v3, v8, v3, s[4:5]
	s_mov_b32 s11, s8
	s_mov_b32 s12, s8
	s_waitcnt lgkmcnt(2)
	v_mfma_f32_32x32x16_f16 v[64:79], v[200:203], v[0:3], 0
	ds_read2_b32 v[2:3], v224 offset0:2 offset1:3
	ds_read2_b32 v[0:1], v224 offset1:1
	ds_read2_b32 v[16:17], v225 offset1:1
	ds_read2_b32 v[18:19], v225 offset0:2 offset1:3
	s_mov_b32 s13, s8
	s_mov_b32 s14, s8
	s_mov_b32 s15, s8
	s_waitcnt lgkmcnt(3)
	v_or_b32_sdwa v8, v3, s34 dst_sel:DWORD dst_unused:UNUSED_PAD src0_sel:WORD_0 src1_sel:DWORD
	s_waitcnt lgkmcnt(0)
	v_or_b32_sdwa v20, v19, s34 dst_sel:DWORD dst_unused:UNUSED_PAD src0_sel:WORD_0 src1_sel:DWORD
	v_cndmask_b32_e64 v19, v20, v19, s[4:5]
	v_cndmask_b32_e64 v3, v8, v3, s[4:5]
	s_mov_b32 s16, s8
	v_mfma_f32_32x32x16_f16 v[16:31], v[200:203], v[16:19], 0
	s_mov_b32 s17, s8
	s_mov_b32 s18, s8
	s_mov_b32 s19, s8
	s_mov_b32 s20, s8
	s_mov_b32 s21, s8
	s_mov_b32 s22, s8
	s_mov_b32 s23, s8
	v_mfma_f32_32x32x16_f16 v[48:63], v[200:203], v[0:3], 0
	v_or_b32_sdwa v0, v7, s34 dst_sel:DWORD dst_unused:UNUSED_PAD src0_sel:WORD_0 src1_sel:DWORD
	v_cndmask_b32_e64 v7, v0, v7, s[4:5]
	s_nop 1
	v_mfma_f32_32x32x16_f16 v[32:47], v[200:203], v[4:7], 0
	v_mov_b64_e32 v[0:1], s[8:9]
	v_mov_b64_e32 v[2:3], s[10:11]
	v_mov_b64_e32 v[4:5], s[12:13]
	v_mov_b64_e32 v[6:7], s[14:15]
	v_mov_b64_e32 v[8:9], s[16:17]
	v_mov_b64_e32 v[10:11], s[18:19]
	v_mov_b64_e32 v[12:13], s[20:21]
	v_mov_b64_e32 v[14:15], s[22:23]
	s_nop 15
	s_nop 3
	v_cvt_pk_f16_f32 v239, v64, v65
	v_cvt_pk_f16_f32 v240, v66, v67
	v_and_b32 v209, s35, v239
	v_and_b32 v238, s35, v240
	v_pk_fma_f16 v236, v209, s42, v227
	v_pk_fma_f16 v237, v238, s42, v227
	v_pk_fma_f16 v236, v236, v209, s43
	v_pk_fma_f16 v237, v237, v238, s43
	v_pk_mul_f16 v236, v236, v209
	v_pk_mul_f16 v237, v237, v238
	v_exp_f16_sdwa v236, v236 dst_sel:WORD_0 dst_unused:UNUSED_PRESERVE src0_sel:WORD_0
	v_exp_f16_sdwa v237, v237 dst_sel:WORD_0 dst_unused:UNUSED_PRESERVE src0_sel:WORD_0
	v_exp_f16_sdwa v236, v236 dst_sel:WORD_1 dst_unused:UNUSED_PRESERVE src0_sel:WORD_1
	v_exp_f16_sdwa v237, v237 dst_sel:WORD_1 dst_unused:UNUSED_PRESERVE src0_sel:WORD_1
	v_pk_add_f16 v64, v239, v209
	v_pk_add_f16 v65, v240, v238
	v_pk_fma_f16 v236, v209, v236, v64 neg_lo:[1,0,0] neg_hi:[1,0,0]
	v_pk_fma_f16 v237, v238, v237, v65 neg_lo:[1,0,0] neg_hi:[1,0,0]
	v_cvt_pk_f16_f32 v209, v68, v69
	v_cvt_pk_f16_f32 v238, v70, v71
	v_and_b32 v66, s35, v209
	v_and_b32 v67, s35, v238
	v_pk_fma_f16 v64, v66, s42, v227
	v_pk_fma_f16 v65, v67, s42, v227
	v_pk_fma_f16 v64, v64, v66, s43
	v_pk_fma_f16 v65, v65, v67, s43
	v_pk_mul_f16 v64, v64, v66
	v_pk_mul_f16 v65, v65, v67
	v_exp_f16_sdwa v64, v64 dst_sel:WORD_0 dst_unused:UNUSED_PRESERVE src0_sel:WORD_0
	v_exp_f16_sdwa v65, v65 dst_sel:WORD_0 dst_unused:UNUSED_PRESERVE src0_sel:WORD_0
	v_exp_f16_sdwa v64, v64 dst_sel:WORD_1 dst_unused:UNUSED_PRESERVE src0_sel:WORD_1
	v_exp_f16_sdwa v65, v65 dst_sel:WORD_1 dst_unused:UNUSED_PRESERVE src0_sel:WORD_1
	v_pk_add_f16 v68, v209, v66
	v_pk_add_f16 v69, v238, v67
	v_pk_fma_f16 v64, v66, v64, v68 neg_lo:[1,0,0] neg_hi:[1,0,0]
	v_pk_fma_f16 v65, v67, v65, v69 neg_lo:[1,0,0] neg_hi:[1,0,0]
	v_cvt_pk_f16_f32 v70, v72, v73
	v_cvt_pk_f16_f32 v71, v74, v75
	v_and_b32 v68, s35, v70
	v_and_b32 v69, s35, v71
	v_pk_fma_f16 v66, v68, s42, v227
	v_pk_fma_f16 v67, v69, s42, v227
	v_pk_fma_f16 v66, v66, v68, s43
	v_pk_fma_f16 v67, v67, v69, s43
	v_pk_mul_f16 v66, v66, v68
	v_pk_mul_f16 v67, v67, v69
	v_exp_f16_sdwa v66, v66 dst_sel:WORD_0 dst_unused:UNUSED_PRESERVE src0_sel:WORD_0
	v_exp_f16_sdwa v67, v67 dst_sel:WORD_0 dst_unused:UNUSED_PRESERVE src0_sel:WORD_0
	v_exp_f16_sdwa v66, v66 dst_sel:WORD_1 dst_unused:UNUSED_PRESERVE src0_sel:WORD_1
	v_exp_f16_sdwa v67, v67 dst_sel:WORD_1 dst_unused:UNUSED_PRESERVE src0_sel:WORD_1
	v_pk_add_f16 v72, v70, v68
	v_pk_add_f16 v73, v71, v69
	v_pk_fma_f16 v66, v68, v66, v72 neg_lo:[1,0,0] neg_hi:[1,0,0]
	v_pk_fma_f16 v67, v69, v67, v73 neg_lo:[1,0,0] neg_hi:[1,0,0]
	v_cvt_pk_f16_f32 v72, v76, v77
	v_cvt_pk_f16_f32 v73, v78, v79
	v_and_b32 v70, s35, v72
	v_and_b32 v71, s35, v73
	v_pk_fma_f16 v68, v70, s42, v227
	v_pk_fma_f16 v69, v71, s42, v227
	v_pk_fma_f16 v68, v68, v70, s43
	v_pk_fma_f16 v69, v69, v71, s43
	v_pk_mul_f16 v68, v68, v70
	v_pk_mul_f16 v69, v69, v71
	v_exp_f16_sdwa v68, v68 dst_sel:WORD_0 dst_unused:UNUSED_PRESERVE src0_sel:WORD_0
	v_exp_f16_sdwa v69, v69 dst_sel:WORD_0 dst_unused:UNUSED_PRESERVE src0_sel:WORD_0
	v_exp_f16_sdwa v68, v68 dst_sel:WORD_1 dst_unused:UNUSED_PRESERVE src0_sel:WORD_1
	v_exp_f16_sdwa v69, v69 dst_sel:WORD_1 dst_unused:UNUSED_PRESERVE src0_sel:WORD_1
	v_pk_add_f16 v74, v72, v70
	v_pk_add_f16 v75, v73, v71
	v_pk_fma_f16 v68, v70, v68, v74 neg_lo:[1,0,0] neg_hi:[1,0,0]
	v_pk_fma_f16 v69, v71, v69, v75 neg_lo:[1,0,0] neg_hi:[1,0,0]
	v_cvt_pk_f16_f32 v74, v48, v49
	v_cvt_pk_f16_f32 v75, v50, v51
	v_and_b32 v72, s35, v74
	v_and_b32 v73, s35, v75
	v_pk_fma_f16 v70, v72, s42, v227
	v_pk_fma_f16 v71, v73, s42, v227
	v_pk_fma_f16 v70, v70, v72, s43
	v_pk_fma_f16 v71, v71, v73, s43
	v_pk_mul_f16 v70, v70, v72
	v_pk_mul_f16 v71, v71, v73
	v_exp_f16_sdwa v70, v70 dst_sel:WORD_0 dst_unused:UNUSED_PRESERVE src0_sel:WORD_0
	v_exp_f16_sdwa v71, v71 dst_sel:WORD_0 dst_unused:UNUSED_PRESERVE src0_sel:WORD_0
	v_exp_f16_sdwa v70, v70 dst_sel:WORD_1 dst_unused:UNUSED_PRESERVE src0_sel:WORD_1
	v_exp_f16_sdwa v71, v71 dst_sel:WORD_1 dst_unused:UNUSED_PRESERVE src0_sel:WORD_1
	v_pk_add_f16 v48, v74, v72
	v_pk_add_f16 v49, v75, v73
	v_pk_fma_f16 v70, v72, v70, v48 neg_lo:[1,0,0] neg_hi:[1,0,0]
	v_pk_fma_f16 v71, v73, v71, v49 neg_lo:[1,0,0] neg_hi:[1,0,0]
	v_cvt_pk_f16_f32 v72, v52, v53
	v_cvt_pk_f16_f32 v73, v54, v55
	v_and_b32 v50, s35, v72
	v_and_b32 v51, s35, v73
	v_pk_fma_f16 v48, v50, s42, v227
	v_pk_fma_f16 v49, v51, s42, v227
	v_pk_fma_f16 v48, v48, v50, s43
	v_pk_fma_f16 v49, v49, v51, s43
	v_pk_mul_f16 v48, v48, v50
	v_pk_mul_f16 v49, v49, v51
	v_exp_f16_sdwa v48, v48 dst_sel:WORD_0 dst_unused:UNUSED_PRESERVE src0_sel:WORD_0
	v_exp_f16_sdwa v49, v49 dst_sel:WORD_0 dst_unused:UNUSED_PRESERVE src0_sel:WORD_0
	v_exp_f16_sdwa v48, v48 dst_sel:WORD_1 dst_unused:UNUSED_PRESERVE src0_sel:WORD_1
	v_exp_f16_sdwa v49, v49 dst_sel:WORD_1 dst_unused:UNUSED_PRESERVE src0_sel:WORD_1
	v_pk_add_f16 v52, v72, v50
	v_pk_add_f16 v53, v73, v51
	v_pk_fma_f16 v48, v50, v48, v52 neg_lo:[1,0,0] neg_hi:[1,0,0]
	v_pk_fma_f16 v49, v51, v49, v53 neg_lo:[1,0,0] neg_hi:[1,0,0]
	v_cvt_pk_f16_f32 v54, v56, v57
	v_cvt_pk_f16_f32 v55, v58, v59
	v_and_b32 v52, s35, v54
	v_and_b32 v53, s35, v55
	v_pk_fma_f16 v50, v52, s42, v227
	v_pk_fma_f16 v51, v53, s42, v227
	v_pk_fma_f16 v50, v50, v52, s43
	v_pk_fma_f16 v51, v51, v53, s43
	v_pk_mul_f16 v50, v50, v52
	v_pk_mul_f16 v51, v51, v53
	v_exp_f16_sdwa v50, v50 dst_sel:WORD_0 dst_unused:UNUSED_PRESERVE src0_sel:WORD_0
	v_exp_f16_sdwa v51, v51 dst_sel:WORD_0 dst_unused:UNUSED_PRESERVE src0_sel:WORD_0
	v_exp_f16_sdwa v50, v50 dst_sel:WORD_1 dst_unused:UNUSED_PRESERVE src0_sel:WORD_1
	v_exp_f16_sdwa v51, v51 dst_sel:WORD_1 dst_unused:UNUSED_PRESERVE src0_sel:WORD_1
	v_pk_add_f16 v56, v54, v52
	v_pk_add_f16 v57, v55, v53
	v_pk_fma_f16 v50, v52, v50, v56 neg_lo:[1,0,0] neg_hi:[1,0,0]
	v_pk_fma_f16 v51, v53, v51, v57 neg_lo:[1,0,0] neg_hi:[1,0,0]
	v_cvt_pk_f16_f32 v56, v60, v61
	v_cvt_pk_f16_f32 v57, v62, v63
	v_and_b32 v54, s35, v56
	v_and_b32 v55, s35, v57
	v_pk_fma_f16 v52, v54, s42, v227
	v_pk_fma_f16 v53, v55, s42, v227
	v_pk_fma_f16 v52, v52, v54, s43
	v_pk_fma_f16 v53, v53, v55, s43
	v_pk_mul_f16 v52, v52, v54
	v_pk_mul_f16 v53, v53, v55
	v_exp_f16_sdwa v52, v52 dst_sel:WORD_0 dst_unused:UNUSED_PRESERVE src0_sel:WORD_0
	v_exp_f16_sdwa v53, v53 dst_sel:WORD_0 dst_unused:UNUSED_PRESERVE src0_sel:WORD_0
	v_exp_f16_sdwa v52, v52 dst_sel:WORD_1 dst_unused:UNUSED_PRESERVE src0_sel:WORD_1
	v_exp_f16_sdwa v53, v53 dst_sel:WORD_1 dst_unused:UNUSED_PRESERVE src0_sel:WORD_1
	v_pk_add_f16 v58, v56, v54
	v_pk_add_f16 v59, v57, v55
	v_pk_fma_f16 v52, v54, v52, v58 neg_lo:[1,0,0] neg_hi:[1,0,0]
	v_pk_fma_f16 v53, v55, v53, v59 neg_lo:[1,0,0] neg_hi:[1,0,0]
	ds_write2_b64 v228, v[236:237], v[70:71] offset0:78 offset1:142
	ds_write2st64_b64 v231, v[64:65], v[48:49] offset0:5 offset1:6
	ds_write2st64_b64 v232, v[66:67], v[50:51] offset0:9 offset1:10
	ds_write2st64_b64 v233, v[68:69], v[52:53] offset0:13 offset1:14
	v_cvt_pk_f16_f32 v52, v32, v33
	v_cvt_pk_f16_f32 v53, v34, v35
	v_and_b32 v50, s35, v52
	v_and_b32 v51, s35, v53
	v_pk_fma_f16 v48, v50, s42, v227
	v_pk_fma_f16 v49, v51, s42, v227
	v_pk_fma_f16 v48, v48, v50, s43
	v_pk_fma_f16 v49, v49, v51, s43
	v_mov_b32_e32 v237, 0xff800000
	v_pk_mul_f16 v48, v48, v50
	v_pk_mul_f16 v49, v49, v51
	v_exp_f16_sdwa v48, v48 dst_sel:WORD_0 dst_unused:UNUSED_PRESERVE src0_sel:WORD_0
	v_exp_f16_sdwa v49, v49 dst_sel:WORD_0 dst_unused:UNUSED_PRESERVE src0_sel:WORD_0
	v_exp_f16_sdwa v48, v48 dst_sel:WORD_1 dst_unused:UNUSED_PRESERVE src0_sel:WORD_1
	v_exp_f16_sdwa v49, v49 dst_sel:WORD_1 dst_unused:UNUSED_PRESERVE src0_sel:WORD_1
	v_pk_add_f16 v32, v52, v50
	v_pk_add_f16 v33, v53, v51
	v_pk_fma_f16 v48, v50, v48, v32 neg_lo:[1,0,0] neg_hi:[1,0,0]
	v_pk_fma_f16 v49, v51, v49, v33 neg_lo:[1,0,0] neg_hi:[1,0,0]
	v_mov_b32_e32 v236, 0
	v_cvt_pk_f16_f32 v50, v36, v37
	v_cvt_pk_f16_f32 v51, v38, v39
	v_and_b32 v34, s35, v50
	v_and_b32 v35, s35, v51
	v_pk_fma_f16 v32, v34, s42, v227
	v_pk_fma_f16 v33, v35, s42, v227
	v_pk_fma_f16 v32, v32, v34, s43
	v_pk_fma_f16 v33, v33, v35, s43
	v_pk_mul_f16 v32, v32, v34
	v_pk_mul_f16 v33, v33, v35
	v_exp_f16_sdwa v32, v32 dst_sel:WORD_0 dst_unused:UNUSED_PRESERVE src0_sel:WORD_0
	v_exp_f16_sdwa v33, v33 dst_sel:WORD_0 dst_unused:UNUSED_PRESERVE src0_sel:WORD_0
	v_exp_f16_sdwa v32, v32 dst_sel:WORD_1 dst_unused:UNUSED_PRESERVE src0_sel:WORD_1
	v_exp_f16_sdwa v33, v33 dst_sel:WORD_1 dst_unused:UNUSED_PRESERVE src0_sel:WORD_1
	v_pk_add_f16 v36, v50, v34
	v_pk_add_f16 v37, v51, v35
	v_pk_fma_f16 v32, v34, v32, v36 neg_lo:[1,0,0] neg_hi:[1,0,0]
	v_pk_fma_f16 v33, v35, v33, v37 neg_lo:[1,0,0] neg_hi:[1,0,0]
	v_cvt_pk_f16_f32 v38, v40, v41
	v_cvt_pk_f16_f32 v39, v42, v43
	v_and_b32 v36, s35, v38
	v_and_b32 v37, s35, v39
	v_pk_fma_f16 v34, v36, s42, v227
	v_pk_fma_f16 v35, v37, s42, v227
	v_pk_fma_f16 v34, v34, v36, s43
	v_pk_fma_f16 v35, v35, v37, s43
	v_pk_mul_f16 v34, v34, v36
	v_pk_mul_f16 v35, v35, v37
	v_exp_f16_sdwa v34, v34 dst_sel:WORD_0 dst_unused:UNUSED_PRESERVE src0_sel:WORD_0
	v_exp_f16_sdwa v35, v35 dst_sel:WORD_0 dst_unused:UNUSED_PRESERVE src0_sel:WORD_0
	v_exp_f16_sdwa v34, v34 dst_sel:WORD_1 dst_unused:UNUSED_PRESERVE src0_sel:WORD_1
	v_exp_f16_sdwa v35, v35 dst_sel:WORD_1 dst_unused:UNUSED_PRESERVE src0_sel:WORD_1
	v_pk_add_f16 v40, v38, v36
	v_pk_add_f16 v41, v39, v37
	v_pk_fma_f16 v34, v36, v34, v40 neg_lo:[1,0,0] neg_hi:[1,0,0]
	v_pk_fma_f16 v35, v37, v35, v41 neg_lo:[1,0,0] neg_hi:[1,0,0]
	v_cvt_pk_f16_f32 v40, v44, v45
	v_cvt_pk_f16_f32 v41, v46, v47
	v_and_b32 v38, s35, v40
	v_and_b32 v39, s35, v41
	v_pk_fma_f16 v36, v38, s42, v227
	v_pk_fma_f16 v37, v39, s42, v227
	v_pk_fma_f16 v36, v36, v38, s43
	v_pk_fma_f16 v37, v37, v39, s43
	v_pk_mul_f16 v36, v36, v38
	v_pk_mul_f16 v37, v37, v39
	v_exp_f16_sdwa v36, v36 dst_sel:WORD_0 dst_unused:UNUSED_PRESERVE src0_sel:WORD_0
	v_exp_f16_sdwa v37, v37 dst_sel:WORD_0 dst_unused:UNUSED_PRESERVE src0_sel:WORD_0
	v_exp_f16_sdwa v36, v36 dst_sel:WORD_1 dst_unused:UNUSED_PRESERVE src0_sel:WORD_1
	v_exp_f16_sdwa v37, v37 dst_sel:WORD_1 dst_unused:UNUSED_PRESERVE src0_sel:WORD_1
	v_pk_add_f16 v42, v40, v38
	v_pk_add_f16 v43, v41, v39
	v_pk_fma_f16 v36, v38, v36, v42 neg_lo:[1,0,0] neg_hi:[1,0,0]
	v_pk_fma_f16 v37, v39, v37, v43 neg_lo:[1,0,0] neg_hi:[1,0,0]
	v_cvt_pk_f16_f32 v42, v16, v17
	v_cvt_pk_f16_f32 v43, v18, v19
	v_and_b32 v40, s35, v42
	v_and_b32 v41, s35, v43
	v_pk_fma_f16 v38, v40, s42, v227
	v_pk_fma_f16 v39, v41, s42, v227
	v_pk_fma_f16 v38, v38, v40, s43
	v_pk_fma_f16 v39, v39, v41, s43
	v_pk_mul_f16 v38, v38, v40
	v_pk_mul_f16 v39, v39, v41
	v_exp_f16_sdwa v38, v38 dst_sel:WORD_0 dst_unused:UNUSED_PRESERVE src0_sel:WORD_0
	v_exp_f16_sdwa v39, v39 dst_sel:WORD_0 dst_unused:UNUSED_PRESERVE src0_sel:WORD_0
	v_exp_f16_sdwa v38, v38 dst_sel:WORD_1 dst_unused:UNUSED_PRESERVE src0_sel:WORD_1
	v_exp_f16_sdwa v39, v39 dst_sel:WORD_1 dst_unused:UNUSED_PRESERVE src0_sel:WORD_1
	v_pk_add_f16 v16, v42, v40
	v_pk_add_f16 v17, v43, v41
	v_pk_fma_f16 v38, v40, v38, v16 neg_lo:[1,0,0] neg_hi:[1,0,0]
	v_pk_fma_f16 v39, v41, v39, v17 neg_lo:[1,0,0] neg_hi:[1,0,0]
	v_cvt_pk_f16_f32 v40, v20, v21
	v_cvt_pk_f16_f32 v41, v22, v23
	v_and_b32 v18, s35, v40
	v_and_b32 v19, s35, v41
	v_pk_fma_f16 v16, v18, s42, v227
	v_pk_fma_f16 v17, v19, s42, v227
	v_pk_fma_f16 v16, v16, v18, s43
	v_pk_fma_f16 v17, v17, v19, s43
	v_pk_mul_f16 v16, v16, v18
	v_pk_mul_f16 v17, v17, v19
	v_exp_f16_sdwa v16, v16 dst_sel:WORD_0 dst_unused:UNUSED_PRESERVE src0_sel:WORD_0
	v_exp_f16_sdwa v17, v17 dst_sel:WORD_0 dst_unused:UNUSED_PRESERVE src0_sel:WORD_0
	v_exp_f16_sdwa v16, v16 dst_sel:WORD_1 dst_unused:UNUSED_PRESERVE src0_sel:WORD_1
	v_exp_f16_sdwa v17, v17 dst_sel:WORD_1 dst_unused:UNUSED_PRESERVE src0_sel:WORD_1
	v_pk_add_f16 v20, v40, v18
	v_pk_add_f16 v21, v41, v19
	v_pk_fma_f16 v16, v18, v16, v20 neg_lo:[1,0,0] neg_hi:[1,0,0]
	v_pk_fma_f16 v17, v19, v17, v21 neg_lo:[1,0,0] neg_hi:[1,0,0]
	v_cvt_pk_f16_f32 v22, v24, v25
	v_cvt_pk_f16_f32 v23, v26, v27
	v_and_b32 v20, s35, v22
	v_and_b32 v21, s35, v23
	v_pk_fma_f16 v18, v20, s42, v227
	v_pk_fma_f16 v19, v21, s42, v227
	v_pk_fma_f16 v18, v18, v20, s43
	v_pk_fma_f16 v19, v19, v21, s43
	v_pk_mul_f16 v18, v18, v20
	v_pk_mul_f16 v19, v19, v21
	v_exp_f16_sdwa v18, v18 dst_sel:WORD_0 dst_unused:UNUSED_PRESERVE src0_sel:WORD_0
	v_exp_f16_sdwa v19, v19 dst_sel:WORD_0 dst_unused:UNUSED_PRESERVE src0_sel:WORD_0
	v_exp_f16_sdwa v18, v18 dst_sel:WORD_1 dst_unused:UNUSED_PRESERVE src0_sel:WORD_1
	v_exp_f16_sdwa v19, v19 dst_sel:WORD_1 dst_unused:UNUSED_PRESERVE src0_sel:WORD_1
	v_pk_add_f16 v24, v22, v20
	v_pk_add_f16 v25, v23, v21
	v_pk_fma_f16 v18, v20, v18, v24 neg_lo:[1,0,0] neg_hi:[1,0,0]
	v_pk_fma_f16 v19, v21, v19, v25 neg_lo:[1,0,0] neg_hi:[1,0,0]
	v_cvt_pk_f16_f32 v24, v28, v29
	v_cvt_pk_f16_f32 v25, v30, v31
	v_and_b32 v22, s35, v24
	v_and_b32 v23, s35, v25
	v_pk_fma_f16 v20, v22, s42, v227
	v_pk_fma_f16 v21, v23, s42, v227
	v_pk_fma_f16 v20, v20, v22, s43
	v_pk_fma_f16 v21, v21, v23, s43
	v_pk_mul_f16 v20, v20, v22
	v_pk_mul_f16 v21, v21, v23
	v_exp_f16_sdwa v20, v20 dst_sel:WORD_0 dst_unused:UNUSED_PRESERVE src0_sel:WORD_0
	v_exp_f16_sdwa v21, v21 dst_sel:WORD_0 dst_unused:UNUSED_PRESERVE src0_sel:WORD_0
	v_exp_f16_sdwa v20, v20 dst_sel:WORD_1 dst_unused:UNUSED_PRESERVE src0_sel:WORD_1
	v_exp_f16_sdwa v21, v21 dst_sel:WORD_1 dst_unused:UNUSED_PRESERVE src0_sel:WORD_1
	v_pk_add_f16 v26, v24, v22
	v_pk_add_f16 v27, v25, v23
	v_pk_fma_f16 v20, v22, v20, v26 neg_lo:[1,0,0] neg_hi:[1,0,0]
	v_pk_fma_f16 v21, v23, v21, v27 neg_lo:[1,0,0] neg_hi:[1,0,0]
	ds_write2st64_b64 v234, v[48:49], v[38:39] offset0:3 offset1:4
	ds_write2st64_b64 v231, v[32:33], v[16:17] offset0:7 offset1:8
	ds_write2st64_b64 v232, v[34:35], v[18:19] offset0:11 offset1:12
	ds_write2st64_b64 v233, v[36:37], v[20:21] offset0:15 offset1:16
	s_mul_i32 s0, s3, 0x280
	v_add_u32_e32 v44, s0, v248
	ds_read_b128 v[16:19], v44
	ds_read_b128 v[20:23], v44 offset:64
	s_waitcnt vmcnt(2)
	s_branch .LBB0_25

.Lno_pre:
	s_nop 15
	s_nop 3
	v_cvt_pk_f16_f32 v38, v64, v65
	v_cvt_pk_f16_f32 v39, v66, v67
	v_and_b32 v36, s35, v38
	v_and_b32 v37, s35, v39
	v_pk_fma_f16 v238, v36, s42, v227
	v_pk_fma_f16 v239, v37, s42, v227
	v_pk_fma_f16 v238, v238, v36, s43
	v_pk_fma_f16 v239, v239, v37, s43
	v_pk_mul_f16 v238, v238, v36
	v_pk_mul_f16 v239, v239, v37
	v_exp_f16_sdwa v238, v238 dst_sel:WORD_0 dst_unused:UNUSED_PRESERVE src0_sel:WORD_0
	v_exp_f16_sdwa v239, v239 dst_sel:WORD_0 dst_unused:UNUSED_PRESERVE src0_sel:WORD_0
	v_exp_f16_sdwa v238, v238 dst_sel:WORD_1 dst_unused:UNUSED_PRESERVE src0_sel:WORD_1
	v_exp_f16_sdwa v239, v239 dst_sel:WORD_1 dst_unused:UNUSED_PRESERVE src0_sel:WORD_1
	v_pk_add_f16 v40, v38, v36
	v_pk_add_f16 v41, v39, v37
	v_pk_fma_f16 v238, v36, v238, v40 neg_lo:[1,0,0] neg_hi:[1,0,0]
	v_pk_fma_f16 v239, v37, v239, v41 neg_lo:[1,0,0] neg_hi:[1,0,0]
	v_cvt_pk_f16_f32 v38, v68, v69
	v_cvt_pk_f16_f32 v39, v70, v71
	v_and_b32 v36, s35, v38
	v_and_b32 v37, s35, v39
	v_pk_fma_f16 v240, v36, s42, v227
	v_pk_fma_f16 v241, v37, s42, v227
	v_pk_fma_f16 v240, v240, v36, s43
	v_pk_fma_f16 v241, v241, v37, s43
	v_cvt_pk_f16_f32 v243, v72, v73
	v_cvt_pk_f16_f32 v244, v74, v75
	v_and_b32 v209, s35, v243
	v_and_b32 v242, s35, v244
	v_pk_fma_f16 v68, v209, s42, v227
	v_pk_fma_f16 v69, v242, s42, v227
	v_pk_fma_f16 v68, v68, v209, s43
	v_pk_fma_f16 v69, v69, v242, s43
	v_cvt_pk_f16_f32 v74, v76, v77
	v_cvt_pk_f16_f32 v75, v78, v79
	v_and_b32 v72, s35, v74
	v_and_b32 v73, s35, v75
	v_pk_fma_f16 v70, v72, s42, v227
	v_pk_fma_f16 v71, v73, s42, v227
	v_pk_fma_f16 v70, v70, v72, s43
	v_pk_fma_f16 v71, v71, v73, s43
	s_cmp_eq_u32 s8, 0
	v_pk_mul_f16 v240, v240, v36
	v_pk_mul_f16 v241, v241, v37
	v_exp_f16_sdwa v240, v240 dst_sel:WORD_0 dst_unused:UNUSED_PRESERVE src0_sel:WORD_0
	v_exp_f16_sdwa v241, v241 dst_sel:WORD_0 dst_unused:UNUSED_PRESERVE src0_sel:WORD_0
	v_exp_f16_sdwa v240, v240 dst_sel:WORD_1 dst_unused:UNUSED_PRESERVE src0_sel:WORD_1
	v_exp_f16_sdwa v241, v241 dst_sel:WORD_1 dst_unused:UNUSED_PRESERVE src0_sel:WORD_1
	v_pk_add_f16 v40, v38, v36
	v_pk_add_f16 v41, v39, v37
	v_pk_fma_f16 v240, v36, v240, v40 neg_lo:[1,0,0] neg_hi:[1,0,0]
	v_pk_fma_f16 v241, v37, v241, v41 neg_lo:[1,0,0] neg_hi:[1,0,0]
	v_pk_mul_f16 v68, v68, v209
	v_pk_mul_f16 v69, v69, v242
	v_exp_f16_sdwa v68, v68 dst_sel:WORD_0 dst_unused:UNUSED_PRESERVE src0_sel:WORD_0
	v_exp_f16_sdwa v69, v69 dst_sel:WORD_0 dst_unused:UNUSED_PRESERVE src0_sel:WORD_0
	v_exp_f16_sdwa v68, v68 dst_sel:WORD_1 dst_unused:UNUSED_PRESERVE src0_sel:WORD_1
	v_exp_f16_sdwa v69, v69 dst_sel:WORD_1 dst_unused:UNUSED_PRESERVE src0_sel:WORD_1
	v_pk_add_f16 v76, v243, v209
	v_pk_add_f16 v77, v244, v242
	v_pk_fma_f16 v68, v209, v68, v76 neg_lo:[1,0,0] neg_hi:[1,0,0]
	v_pk_fma_f16 v69, v242, v69, v77 neg_lo:[1,0,0] neg_hi:[1,0,0]
	v_pk_mul_f16 v70, v70, v72
	v_pk_mul_f16 v71, v71, v73
	v_exp_f16_sdwa v70, v70 dst_sel:WORD_0 dst_unused:UNUSED_PRESERVE src0_sel:WORD_0
	v_exp_f16_sdwa v71, v71 dst_sel:WORD_0 dst_unused:UNUSED_PRESERVE src0_sel:WORD_0
	v_exp_f16_sdwa v70, v70 dst_sel:WORD_1 dst_unused:UNUSED_PRESERVE src0_sel:WORD_1
	v_exp_f16_sdwa v71, v71 dst_sel:WORD_1 dst_unused:UNUSED_PRESERVE src0_sel:WORD_1
	v_pk_add_f16 v76, v74, v72
	v_pk_add_f16 v77, v75, v73
	v_pk_fma_f16 v70, v72, v70, v76 neg_lo:[1,0,0] neg_hi:[1,0,0]
	v_pk_fma_f16 v71, v73, v71, v77 neg_lo:[1,0,0] neg_hi:[1,0,0]
	v_cvt_pk_f16_f32 v74, v48, v49
	v_cvt_pk_f16_f32 v75, v50, v51
	v_and_b32 v72, s35, v74
	v_and_b32 v73, s35, v75
	v_pk_fma_f16 v64, v72, s42, v227
	v_pk_fma_f16 v65, v73, s42, v227
	v_pk_fma_f16 v64, v64, v72, s43
	v_pk_fma_f16 v65, v65, v73, s43
	v_cvt_pk_f16_f32 v78, v52, v53
	v_cvt_pk_f16_f32 v79, v54, v55
	v_and_b32 v76, s35, v78
	v_and_b32 v77, s35, v79
	v_pk_fma_f16 v66, v76, s42, v227
	v_pk_fma_f16 v67, v77, s42, v227
	v_pk_fma_f16 v66, v66, v76, s43
	v_pk_fma_f16 v67, v67, v77, s43
	v_pk_mul_f16 v64, v64, v72
	v_pk_mul_f16 v65, v65, v73
	v_exp_f16_sdwa v64, v64 dst_sel:WORD_0 dst_unused:UNUSED_PRESERVE src0_sel:WORD_0
	v_exp_f16_sdwa v65, v65 dst_sel:WORD_0 dst_unused:UNUSED_PRESERVE src0_sel:WORD_0
	v_exp_f16_sdwa v64, v64 dst_sel:WORD_1 dst_unused:UNUSED_PRESERVE src0_sel:WORD_1
	v_exp_f16_sdwa v65, v65 dst_sel:WORD_1 dst_unused:UNUSED_PRESERVE src0_sel:WORD_1
	v_pk_add_f16 v209, v74, v72
	v_pk_add_f16 v242, v75, v73
	v_pk_fma_f16 v64, v72, v64, v209 neg_lo:[1,0,0] neg_hi:[1,0,0]
	v_pk_fma_f16 v65, v73, v65, v242 neg_lo:[1,0,0] neg_hi:[1,0,0]
	v_pk_mul_f16 v66, v66, v76
	v_pk_mul_f16 v67, v67, v77
	v_exp_f16_sdwa v66, v66 dst_sel:WORD_0 dst_unused:UNUSED_PRESERVE src0_sel:WORD_0
	v_exp_f16_sdwa v67, v67 dst_sel:WORD_0 dst_unused:UNUSED_PRESERVE src0_sel:WORD_0
	v_exp_f16_sdwa v66, v66 dst_sel:WORD_1 dst_unused:UNUSED_PRESERVE src0_sel:WORD_1
	v_exp_f16_sdwa v67, v67 dst_sel:WORD_1 dst_unused:UNUSED_PRESERVE src0_sel:WORD_1
	v_pk_add_f16 v72, v78, v76
	v_pk_add_f16 v73, v79, v77
	v_pk_fma_f16 v66, v76, v66, v72 neg_lo:[1,0,0] neg_hi:[1,0,0]
	v_pk_fma_f16 v67, v77, v67, v73 neg_lo:[1,0,0] neg_hi:[1,0,0]
	v_cvt_pk_f16_f32 v74, v56, v57
	v_cvt_pk_f16_f32 v75, v58, v59
	v_and_b32 v72, s35, v74
	v_and_b32 v73, s35, v75
	v_pk_fma_f16 v48, v72, s42, v227
	v_pk_fma_f16 v49, v73, s42, v227
	v_pk_fma_f16 v48, v48, v72, s43
	v_pk_fma_f16 v49, v49, v73, s43
	v_cvt_pk_f16_f32 v58, v60, v61
	v_cvt_pk_f16_f32 v59, v62, v63
	v_and_b32 v56, s35, v58
	v_and_b32 v57, s35, v59
	v_pk_fma_f16 v50, v56, s42, v227
	v_pk_fma_f16 v51, v57, s42, v227
	v_pk_fma_f16 v50, v50, v56, s43
	v_pk_fma_f16 v51, v51, v57, s43
	v_pk_mul_f16 v48, v48, v72
	v_pk_mul_f16 v49, v49, v73
	v_exp_f16_sdwa v48, v48 dst_sel:WORD_0 dst_unused:UNUSED_PRESERVE src0_sel:WORD_0
	v_exp_f16_sdwa v49, v49 dst_sel:WORD_0 dst_unused:UNUSED_PRESERVE src0_sel:WORD_0
	v_exp_f16_sdwa v48, v48 dst_sel:WORD_1 dst_unused:UNUSED_PRESERVE src0_sel:WORD_1
	v_exp_f16_sdwa v49, v49 dst_sel:WORD_1 dst_unused:UNUSED_PRESERVE src0_sel:WORD_1
	v_pk_add_f16 v62, v74, v72
	v_pk_add_f16 v63, v75, v73
	v_pk_fma_f16 v48, v72, v48, v62 neg_lo:[1,0,0] neg_hi:[1,0,0]
	v_pk_fma_f16 v49, v73, v49, v63 neg_lo:[1,0,0] neg_hi:[1,0,0]
	v_pk_mul_f16 v50, v50, v56
	v_pk_mul_f16 v51, v51, v57
	v_exp_f16_sdwa v50, v50 dst_sel:WORD_0 dst_unused:UNUSED_PRESERVE src0_sel:WORD_0
	v_exp_f16_sdwa v51, v51 dst_sel:WORD_0 dst_unused:UNUSED_PRESERVE src0_sel:WORD_0
	v_exp_f16_sdwa v50, v50 dst_sel:WORD_1 dst_unused:UNUSED_PRESERVE src0_sel:WORD_1
	v_exp_f16_sdwa v51, v51 dst_sel:WORD_1 dst_unused:UNUSED_PRESERVE src0_sel:WORD_1
	v_pk_add_f16 v62, v58, v56
	v_pk_add_f16 v63, v59, v57
	v_pk_fma_f16 v50, v56, v50, v62 neg_lo:[1,0,0] neg_hi:[1,0,0]
	v_pk_fma_f16 v51, v57, v51, v63 neg_lo:[1,0,0] neg_hi:[1,0,0]
	ds_write2_b64 v246, v[238:239], v[240:241] offset0:136 offset1:138
	ds_write2_b64 v246, v[64:65], v[66:67] offset0:144 offset1:146
	ds_write2_b64 v246, v[68:69], v[70:71] offset0:140 offset1:142
	ds_write2_b64 v246, v[48:49], v[50:51] offset0:148 offset1:150
	ds_read2_b64 v[24:27], v249 offset1:1
	ds_read2_b64 v[28:31], v249 offset0:8 offset1:9
	ds_read2_b64 v[40:43], v250 offset1:1
	ds_read2_b64 v[44:47], v250 offset0:8 offset1:9
	s_waitcnt lgkmcnt(2)
	v_mfma_f32_16x16x32_f16 v[32:35], v[24:27], v[16:19], 0
	v_mfma_f32_16x16x32_f16 v[32:35], v[28:31], v[20:23], v[32:35]
	s_waitcnt lgkmcnt(0)
	v_mfma_f32_16x16x32_f16 v[36:39], v[40:43], v[16:19], 0
	v_mfma_f32_16x16x32_f16 v[36:39], v[44:47], v[20:23], v[36:39]
	s_nop 7
	v_max3_f32 v52, v32, v33, v34
	v_max3_f32 v52, v52, v35, v36
	v_max3_f32 v52, v52, v37, v38
	v_max_f32_e32 v52, v52, v39
	v_mov_b32_e32 v53, v52
	s_nop 1
	v_permlane16_swap_b32_e32 v52, v53
	s_nop 0
	v_max_f32_e32 v52, v52, v53
	v_mov_b32_e32 v53, v52
	s_nop 1
	v_permlane32_swap_b32_e32 v52, v53
	s_nop 0
	v_max_f32_e32 v48, v52, v53
	s_cbranch_scc1 .LBB0_23
	v_add_f32_e32 v49, 0x41000000, v237
	v_cmp_gt_f32_e32 vcc, v48, v49
	s_cbranch_vccz .LBB0_24
	v_max_f32_e32 v48, v48, v48
	v_max_f32_e32 v49, v237, v237
	v_max_f32_e32 v49, v49, v48
	v_sub_f32_e32 v48, v237, v49
	v_exp_f32_e32 v48, v48
	v_mov_b32_e32 v237, v49
	v_pk_mul_f32 v[14:15], v[48:49], v[14:15] op_sel_hi:[0,1]
	v_pk_mul_f32 v[12:13], v[48:49], v[12:13] op_sel_hi:[0,1]
	v_pk_mul_f32 v[10:11], v[48:49], v[10:11] op_sel_hi:[0,1]
	v_pk_mul_f32 v[8:9], v[48:49], v[8:9] op_sel_hi:[0,1]
	v_pk_mul_f32 v[6:7], v[48:49], v[6:7] op_sel_hi:[0,1]
	v_pk_mul_f32 v[4:5], v[48:49], v[4:5] op_sel_hi:[0,1]
	v_pk_mul_f32 v[2:3], v[48:49], v[2:3] op_sel_hi:[0,1]
	v_pk_mul_f32 v[0:1], v[48:49], v[0:1] op_sel_hi:[0,1]
	v_mul_f32_e32 v236, v236, v48
	s_branch .LBB0_24
